# speedup vs baseline: 1.0101x; 1.0083x over previous
.LBB1_13:
	v_mfma_f32_32x32x16_bf16 v[2:17], v[78:81], v[206:209], v[236:251]
	ds_read_b128 v[174:177], v210
	v_add_u32_e32 v195, v230, v228
	v_mfma_f32_32x32x16_bf16 v[2:17], v[74:77], v[190:193], v[2:17]
	ds_read_b128 v[170:173], v210 offset:1024
	v_exp_f32_e32 v199, v28
	v_exp_f32_e32 v198, v32
	v_exp_f32_e32 v197, v20
	v_exp_f32_e32 v196, v24
	v_mfma_f32_32x32x16_bf16 v[2:17], v[70:73], v[158:161], v[2:17]
	ds_read_b128 v[166:169], v210 offset:2048
	v_exp_f32_e32 v18, v18
	v_exp_f32_e32 v22, v22
	v_exp_f32_e32 v24, v26
	v_exp_f32_e32 v26, v30
	v_fma_f32 v20, v197, s12, s12
	v_fma_f32 v28, v196, s12, s12
	v_fma_f32 v30, v199, s12, s12
	v_fma_f32 v32, v198, s12, s12
	v_mfma_f32_32x32x16_bf16 v[2:17], v[66:69], v[142:145], v[2:17]
	ds_read_b128 v[162:165], v210 offset:3072
	v_exp_f32_e32 v19, v19
	v_exp_f32_e32 v23, v23
	v_exp_f32_e32 v27, v27
	v_exp_f32_e32 v31, v31
	v_fmac_f32_e32 v20, v18, v20
	v_fmac_f32_e32 v28, v22, v28
	v_fmac_f32_e32 v30, v24, v30
	v_fmac_f32_e32 v32, v26, v32
	v_mfma_f32_32x32x16_bf16 v[2:17], v[62:65], v[154:157], v[2:17]
	ds_read_b128 v[158:161], v210 offset:4096
	v_add_f32_e32 v22, 1.0, v19
	v_rcp_f32_e32 v19, v20
	v_rcp_f32_e32 v18, v28
	v_add_f32_e32 v20, 1.0, v23
	v_rcp_f32_e32 v191, v30
	v_rcp_f32_e32 v190, v32
	v_mfma_f32_32x32x16_bf16 v[2:17], v[58:61], v[182:185], v[2:17]
	ds_read_b128 v[154:157], v210 offset:5120
	v_exp_f32_e32 v206, v21
	v_exp_f32_e32 v207, v25
	v_add_f32_e32 v23, 1.0, v27
	v_rcp_f32_e32 v192, v20
	v_add_f32_e32 v20, 1.0, v31
	v_rcp_f32_e32 v193, v22
	v_mfma_f32_32x32x16_bf16 v[2:17], v[54:57], v[186:189], v[2:17]
	ds_read_b128 v[142:145], v210 offset:6144
	v_exp_f32_e32 v208, v29
	v_exp_f32_e32 v209, v33
	v_rcp_f32_e32 v183, v23
	v_rcp_f32_e32 v182, v20
	v_mfma_f32_32x32x16_bf16 v[2:17], v[50:53], v[134:137], v[2:17]
	ds_read_b128 v[130:133], v210 offset:7168
	v_fma_f32 v186, -v196, v18, v18
	v_fma_f32 v187, -v197, v19, v19
	ds_read_b128 v[18:21], v231 offset:36928
	ds_read_b128 v[22:25], v231 offset:36944
	ds_read_b128 v[26:29], v231 offset:36960
	ds_read_b128 v[30:33], v231 offset:36976
	v_pk_fma_f32 v[200:201], v[192:193], v[220:221], v[186:187]
	v_pk_fma_f32 v[134:135], v[198:199], v[190:191], v[190:191] neg_lo:[1,0,0] neg_hi:[1,0,0]
	s_nop 0
	v_pk_fma_f32 v[198:199], v[182:183], v[222:223], v[134:135]
	v_mfma_f32_32x32x16_bf16 v[2:17], v[46:49], v[138:141], v[2:17]
	ds_read_b128 v[134:137], v195 offset:16384
	v_add_f32_e32 v182, 1.0, v206
	v_exp_f32_e32 v183, v201
	v_exp_f32_e32 v186, v200
	v_exp_f32_e32 v187, v199
	v_exp_f32_e32 v188, v198
	v_add_f32_e32 v189, 1.0, v207
	v_add_f32_e32 v190, 1.0, v208
	v_add_f32_e32 v191, 1.0, v209
	v_mfma_f32_32x32x16_bf16 v[2:17], v[42:45], v[146:149], v[2:17]
	ds_read_b128 v[138:141], v195 offset:16416
	v_fmac_f32_e32 v182, v182, v183
	v_fmac_f32_e32 v189, v189, v186
	v_fmac_f32_e32 v190, v190, v187
	v_fmac_f32_e32 v191, v191, v188
	v_mfma_f32_32x32x16_bf16 v[2:17], v[38:41], v[150:153], v[2:17]
	ds_read_b128 v[146:149], v195 offset:16448
	v_rcp_f32_e32 v182, v182
	v_rcp_f32_e32 v189, v189
	v_mfma_f32_32x32x16_bf16 v[2:17], v[34:37], v[178:181], v[2:17]
	ds_read_b128 v[150:153], v195 offset:16480
	v_rcp_f32_e32 v190, v190
	v_rcp_f32_e32 v191, v191
	v_fma_f32 v182, -v183, v182, v182
	v_fma_f32 v183, -v186, v189, v189
	s_waitcnt lgkmcnt(4)
	v_mfma_f32_32x32x16_bf16 v[18:33], v[126:129], v[174:177], v[18:33]
	v_fma_f32 v186, -v187, v190, v190
	v_fma_f32 v187, -v188, v191, v191
	v_cvt_pk_bf16_f32 v252, v182, v183
	v_cvt_pk_bf16_f32 v253, v186, v187
	v_mfma_f32_32x32x16_bf16 v[18:33], v[122:125], v[170:173], v[18:33]
	s_nop 1
	v_exp_f32_e32 v179, v4
	v_exp_f32_e32 v178, v8
	v_exp_f32_e32 v181, v12
	v_exp_f32_e32 v180, v16
	v_mfma_f32_32x32x16_bf16 v[18:33], v[118:121], v[166:169], v[18:33]
	v_exp_f32_e32 v2, v2
	v_exp_f32_e32 v6, v6
	v_exp_f32_e32 v10, v10
	v_exp_f32_e32 v12, v14
	v_fma_f32 v4, v179, s12, s12
	v_fma_f32 v8, v178, s12, s12
	v_fma_f32 v14, v181, s12, s12
	v_fma_f32 v16, v180, s12, s12
	v_mfma_f32_32x32x16_bf16 v[18:33], v[114:117], v[162:165], v[18:33]
	v_exp_f32_e32 v3, v3
	v_fmac_f32_e32 v4, v2, v4
	v_exp_f32_e32 v2, v7
	v_fmac_f32_e32 v8, v6, v8
	v_exp_f32_e32 v6, v11
	v_exp_f32_e32 v7, v15
	v_fmac_f32_e32 v14, v10, v14
	v_fmac_f32_e32 v16, v12, v16
	v_mfma_f32_32x32x16_bf16 v[18:33], v[110:113], v[158:161], v[18:33]
	v_add_f32_e32 v10, 1.0, v3
	v_rcp_f32_e32 v3, v4
	v_add_f32_e32 v4, 1.0, v2
	v_rcp_f32_e32 v2, v8
	v_rcp_f32_e32 v183, v14
	v_rcp_f32_e32 v182, v16
	v_mfma_f32_32x32x16_bf16 v[18:33], v[106:109], v[154:157], v[18:33]
	v_add_f32_e32 v6, 1.0, v6
	v_add_f32_e32 v7, 1.0, v7
	v_rcp_f32_e32 v187, v10
	v_rcp_f32_e32 v186, v4
	v_exp_f32_e32 v190, v5
	v_exp_f32_e32 v191, v9
	v_mfma_f32_32x32x16_bf16 v[18:33], v[102:105], v[142:145], v[18:33]
	v_rcp_f32_e32 v189, v6
	v_rcp_f32_e32 v188, v7
	v_exp_f32_e32 v192, v13
	v_exp_f32_e32 v193, v17
	v_mfma_f32_32x32x16_bf16 v[18:33], v[98:101], v[130:133], v[18:33]
	v_fma_f32 v178, -v178, v2, v2
	v_fma_f32 v179, -v179, v3, v3
	v_pk_fma_f32 v[206:207], v[186:187], v[216:217], v[178:179]
	s_nop 0
	v_pk_fma_f32 v[178:179], v[180:181], v[182:183], v[182:183] neg_lo:[1,0,0] neg_hi:[1,0,0]
	s_nop 0
	v_pk_fma_f32 v[208:209], v[188:189], v[218:219], v[178:179]
	s_waitcnt lgkmcnt(0)
	v_mfma_f32_32x32x16_bf16 v[18:33], v[94:97], v[134:137], v[18:33]
	v_add_f32_e32 v178, 1.0, v190
	v_exp_f32_e32 v179, v207
	v_add_f32_e32 v180, 1.0, v191
	v_exp_f32_e32 v181, v206
	v_exp_f32_e32 v182, v209
	v_exp_f32_e32 v183, v208
	v_add_f32_e32 v184, 1.0, v192
	v_add_f32_e32 v185, 1.0, v193
	v_mfma_f32_32x32x16_bf16 v[18:33], v[90:93], v[138:141], v[18:33]
	v_fmac_f32_e32 v178, v178, v179
	v_fmac_f32_e32 v180, v180, v181
	v_fmac_f32_e32 v184, v184, v182
	v_fmac_f32_e32 v185, v185, v183
	v_mfma_f32_32x32x16_bf16 v[18:33], v[86:89], v[146:149], v[18:33]
	v_rcp_f32_e32 v178, v178
	v_rcp_f32_e32 v180, v180
	v_rcp_f32_e32 v184, v184
	v_rcp_f32_e32 v185, v185
	v_mfma_f32_32x32x16_bf16 v[18:33], v[82:85], v[150:153], v[18:33]
	v_fma_f32 v178, -v179, v178, v178
	v_fma_f32 v179, -v181, v180, v180
	v_fma_f32 v180, -v182, v184, v184
	v_fma_f32 v181, -v183, v185, v185
	v_cvt_pk_bf16_f32 v254, v178, v179
	v_cvt_pk_bf16_f32 v255, v180, v181
	ds_write_b128 v211, v[252:255] offset:8192
	s_waitcnt lgkmcnt(0)
	s_barrier
	s_add_i32 s1, s1, 2
	s_cmp_gt_u32 s1, 16
	v_add_u32_e32 v232, 0x200, v232
	s_cbranch_scc1 .LBB1_30
.LBB1_14:
	v_mfma_f32_32x32x16_bf16 v[2:17], v[78:81], v[174:177], v[236:251]
	v_add_u32_e32 v192, v230, v229
	ds_read2_b32 v[228:229], v232 offset1:32
	ds_read_b128 v[194:197], v210 offset:8192
	v_mfma_f32_32x32x16_bf16 v[2:17], v[74:77], v[170:173], v[2:17]
	ds_read_b128 v[178:181], v210 offset:9216
	v_exp_f32_e32 v187, v20
	v_exp_f32_e32 v186, v24
	v_exp_f32_e32 v189, v28
	v_exp_f32_e32 v188, v32
	v_mfma_f32_32x32x16_bf16 v[2:17], v[70:73], v[166:169], v[2:17]
	ds_read_b128 v[170:173], v210 offset:10240
	v_exp_f32_e32 v18, v18
	v_exp_f32_e32 v22, v22
	v_exp_f32_e32 v24, v26
	v_exp_f32_e32 v26, v30
	v_fma_f32 v20, v187, s12, s12
	v_fma_f32 v28, v186, s12, s12
	v_fma_f32 v30, v189, s12, s12
	v_fma_f32 v32, v188, s12, s12
	v_mfma_f32_32x32x16_bf16 v[2:17], v[66:69], v[162:165], v[2:17]
	ds_read_b128 v[166:169], v210 offset:11264
	v_exp_f32_e32 v19, v19
	v_exp_f32_e32 v23, v23
	v_exp_f32_e32 v27, v27
	v_exp_f32_e32 v31, v31
	v_fmac_f32_e32 v20, v18, v20
	v_fmac_f32_e32 v28, v22, v28
	v_fmac_f32_e32 v30, v24, v30
	v_fmac_f32_e32 v32, v26, v32
	v_mfma_f32_32x32x16_bf16 v[2:17], v[62:65], v[158:161], v[2:17]
	ds_read_b128 v[162:165], v210 offset:12288
	v_add_f32_e32 v22, 1.0, v19
	v_rcp_f32_e32 v19, v20
	v_rcp_f32_e32 v18, v28
	v_rcp_f32_e32 v191, v30
	v_rcp_f32_e32 v190, v32
	v_add_f32_e32 v20, 1.0, v23
	v_mfma_f32_32x32x16_bf16 v[2:17], v[58:61], v[154:157], v[2:17]
	ds_read_b128 v[174:177], v210 offset:13312
	v_rcp_f32_e32 v159, v22
	v_rcp_f32_e32 v158, v20
	v_exp_f32_e32 v160, v21
	v_exp_f32_e32 v161, v25
	v_add_f32_e32 v23, 1.0, v27
	v_add_f32_e32 v20, 1.0, v31
	v_mfma_f32_32x32x16_bf16 v[2:17], v[54:57], v[142:145], v[2:17]
	ds_read_b128 v[182:185], v210 offset:14336
	v_rcp_f32_e32 v155, v23
	v_rcp_f32_e32 v154, v20
	v_exp_f32_e32 v193, v29
	v_exp_f32_e32 v217, v33
	v_mfma_f32_32x32x16_bf16 v[2:17], v[50:53], v[130:133], v[2:17]
	ds_read_b128 v[142:145], v210 offset:15360
	v_fma_f32 v156, -v186, v18, v18
	v_fma_f32 v157, -v187, v19, v19
	ds_read_b128 v[18:21], v231 offset:36928
	ds_read_b128 v[22:25], v231 offset:36944
	ds_read_b128 v[26:29], v231 offset:36960
	ds_read_b128 v[30:33], v231 offset:36976
	v_pk_fma_f32 v[214:215], v[158:159], v[214:215], v[156:157]
	v_pk_fma_f32 v[130:131], v[188:189], v[190:191], v[190:191] neg_lo:[1,0,0] neg_hi:[1,0,0]
	s_nop 0
	v_pk_fma_f32 v[212:213], v[154:155], v[212:213], v[130:131]
	v_mfma_f32_32x32x16_bf16 v[2:17], v[46:49], v[134:137], v[2:17]
	ds_read_b128 v[154:157], v192 offset:16384
	v_add_f32_e32 v130, 1.0, v160
	v_exp_f32_e32 v131, v215
	v_exp_f32_e32 v132, v214
	v_exp_f32_e32 v133, v213
	v_exp_f32_e32 v220, v212
	v_add_f32_e32 v134, 1.0, v161
	v_add_f32_e32 v135, 1.0, v193
	v_add_f32_e32 v136, 1.0, v217
	v_mfma_f32_32x32x16_bf16 v[2:17], v[42:45], v[138:141], v[2:17]
	ds_read_b128 v[158:161], v192 offset:16416
	v_fmac_f32_e32 v130, v130, v131
	v_fmac_f32_e32 v134, v134, v132
	v_fmac_f32_e32 v135, v135, v133
	v_fmac_f32_e32 v136, v136, v220
	v_mfma_f32_32x32x16_bf16 v[2:17], v[38:41], v[146:149], v[2:17]
	ds_read_b128 v[186:189], v192 offset:16448
	v_rcp_f32_e32 v130, v130
	v_rcp_f32_e32 v134, v134
	v_mfma_f32_32x32x16_bf16 v[2:17], v[34:37], v[150:153], v[2:17]
	ds_read_b128 v[190:193], v192 offset:16480
	v_rcp_f32_e32 v135, v135
	v_rcp_f32_e32 v136, v136
	v_fma_f32 v130, -v131, v130, v130
	v_fma_f32 v131, -v132, v134, v134
	s_waitcnt lgkmcnt(4)
	v_mfma_f32_32x32x16_bf16 v[18:33], v[126:129], v[194:197], v[18:33]
	v_fma_f32 v132, -v133, v135, v135
	v_fma_f32 v133, -v220, v136, v136
	v_cvt_pk_bf16_f32 v252, v130, v131
	v_cvt_pk_bf16_f32 v253, v132, v133
	v_mfma_f32_32x32x16_bf16 v[18:33], v[122:125], v[178:181], v[18:33]
	s_nop 1
	v_exp_f32_e32 v131, v4
	v_exp_f32_e32 v130, v8
	v_exp_f32_e32 v133, v12
	v_exp_f32_e32 v132, v16
	v_mfma_f32_32x32x16_bf16 v[18:33], v[118:121], v[170:173], v[18:33]
	v_exp_f32_e32 v2, v2
	v_exp_f32_e32 v6, v6
	v_exp_f32_e32 v10, v10
	v_exp_f32_e32 v12, v14
	v_fma_f32 v4, v131, s12, s12
	v_fma_f32 v8, v130, s12, s12
	v_fma_f32 v14, v133, s12, s12
	v_fma_f32 v16, v132, s12, s12
	v_mfma_f32_32x32x16_bf16 v[18:33], v[114:117], v[166:169], v[18:33]
	v_exp_f32_e32 v3, v3
	v_fmac_f32_e32 v4, v2, v4
	v_exp_f32_e32 v2, v7
	v_fmac_f32_e32 v8, v6, v8
	v_exp_f32_e32 v6, v11
	v_exp_f32_e32 v7, v15
	v_fmac_f32_e32 v14, v10, v14
	v_fmac_f32_e32 v16, v12, v16
	v_mfma_f32_32x32x16_bf16 v[18:33], v[110:113], v[162:165], v[18:33]
	v_add_f32_e32 v10, 1.0, v3
	v_rcp_f32_e32 v3, v4
	v_add_f32_e32 v4, 1.0, v2
	v_rcp_f32_e32 v2, v8
	v_rcp_f32_e32 v135, v14
	v_rcp_f32_e32 v134, v16
	v_mfma_f32_32x32x16_bf16 v[18:33], v[106:109], v[174:177], v[18:33]
	v_add_f32_e32 v6, 1.0, v6
	v_add_f32_e32 v7, 1.0, v7
	v_rcp_f32_e32 v137, v10
	v_rcp_f32_e32 v136, v4
	v_exp_f32_e32 v140, v5
	v_exp_f32_e32 v141, v9
	v_mfma_f32_32x32x16_bf16 v[18:33], v[102:105], v[182:185], v[18:33]
	v_rcp_f32_e32 v139, v6
	v_rcp_f32_e32 v138, v7
	v_exp_f32_e32 v146, v13
	v_exp_f32_e32 v147, v17
	v_mfma_f32_32x32x16_bf16 v[18:33], v[98:101], v[142:145], v[18:33]
	v_fma_f32 v130, -v130, v2, v2
	v_fma_f32 v131, -v131, v3, v3
	v_pk_fma_f32 v[224:225], v[136:137], v[204:205], v[130:131]
	s_nop 0
	v_pk_fma_f32 v[130:131], v[132:133], v[134:135], v[134:135] neg_lo:[1,0,0] neg_hi:[1,0,0]
	s_nop 0
	v_pk_fma_f32 v[226:227], v[138:139], v[202:203], v[130:131]
	s_waitcnt lgkmcnt(0)
	v_mfma_f32_32x32x16_bf16 v[18:33], v[94:97], v[154:157], v[18:33]
	v_add_f32_e32 v130, 1.0, v140
	v_exp_f32_e32 v131, v225
	v_add_f32_e32 v132, 1.0, v141
	v_exp_f32_e32 v133, v224
	v_exp_f32_e32 v134, v227
	v_exp_f32_e32 v135, v226
	v_add_f32_e32 v136, 1.0, v146
	v_add_f32_e32 v137, 1.0, v147
	v_mfma_f32_32x32x16_bf16 v[18:33], v[90:93], v[158:161], v[18:33]
	v_fmac_f32_e32 v130, v130, v131
	v_fmac_f32_e32 v132, v132, v133
	v_fmac_f32_e32 v136, v136, v134
	v_fmac_f32_e32 v137, v137, v135
	v_mfma_f32_32x32x16_bf16 v[18:33], v[86:89], v[186:189], v[18:33]
	v_rcp_f32_e32 v130, v130
	v_rcp_f32_e32 v132, v132
	v_rcp_f32_e32 v136, v136
	v_rcp_f32_e32 v137, v137
	v_mfma_f32_32x32x16_bf16 v[18:33], v[82:85], v[190:193], v[18:33]
	v_fma_f32 v130, -v131, v130, v130
	v_fma_f32 v131, -v133, v132, v132
	v_fma_f32 v132, -v134, v136, v136
	v_fma_f32 v133, -v135, v137, v137
	v_cvt_pk_bf16_f32 v254, v130, v131
	v_cvt_pk_bf16_f32 v255, v132, v133
	ds_write_b128 v211, v[252:255] offset:0
	s_waitcnt lgkmcnt(0)
	s_barrier
	v_mfma_f32_32x32x16_bf16 v[2:17], v[78:81], v[194:197], v[236:251]
	ds_read_b128 v[202:205], v210
	v_add_u32_e32 v216, v230, v228
	v_mfma_f32_32x32x16_bf16 v[2:17], v[74:77], v[178:181], v[2:17]
	ds_read_b128 v[194:197], v210 offset:1024
	v_exp_f32_e32 v147, v20
	v_exp_f32_e32 v146, v24
	v_exp_f32_e32 v149, v28
	v_exp_f32_e32 v148, v32
	v_mfma_f32_32x32x16_bf16 v[2:17], v[70:73], v[170:173], v[2:17]
	ds_read_b128 v[138:141], v210 offset:2048
	v_exp_f32_e32 v18, v18
	v_exp_f32_e32 v22, v22
	v_exp_f32_e32 v24, v26
	v_exp_f32_e32 v26, v30
	v_fma_f32 v20, v147, s12, s12
	v_fma_f32 v28, v146, s12, s12
	v_fma_f32 v30, v149, s12, s12
	v_fma_f32 v32, v148, s12, s12
	v_mfma_f32_32x32x16_bf16 v[2:17], v[66:69], v[166:169], v[2:17]
	ds_read_b128 v[134:137], v210 offset:3072
	v_exp_f32_e32 v19, v19
	v_exp_f32_e32 v23, v23
	v_exp_f32_e32 v27, v27
	v_exp_f32_e32 v31, v31
	v_fmac_f32_e32 v20, v18, v20
	v_fmac_f32_e32 v28, v22, v28
	v_fmac_f32_e32 v30, v24, v30
	v_fmac_f32_e32 v32, v26, v32
	v_mfma_f32_32x32x16_bf16 v[2:17], v[62:65], v[162:165], v[2:17]
	ds_read_b128 v[166:169], v210 offset:4096
	v_add_f32_e32 v22, 1.0, v19
	v_rcp_f32_e32 v19, v20
	v_rcp_f32_e32 v18, v28
	v_rcp_f32_e32 v151, v30
	v_rcp_f32_e32 v150, v32
	v_add_f32_e32 v20, 1.0, v23
	v_mfma_f32_32x32x16_bf16 v[2:17], v[58:61], v[174:177], v[2:17]
	ds_read_b128 v[162:165], v210 offset:5120
	v_rcp_f32_e32 v153, v22
	v_rcp_f32_e32 v152, v20
	v_add_f32_e32 v23, 1.0, v27
	v_add_f32_e32 v20, 1.0, v31
	v_exp_f32_e32 v180, v21
	v_exp_f32_e32 v181, v25
	v_mfma_f32_32x32x16_bf16 v[2:17], v[54:57], v[182:185], v[2:17]
	ds_read_b128 v[170:173], v210 offset:6144
	v_rcp_f32_e32 v175, v23
	v_rcp_f32_e32 v174, v20
	v_exp_f32_e32 v176, v29
	v_exp_f32_e32 v177, v33
	v_mfma_f32_32x32x16_bf16 v[2:17], v[50:53], v[142:145], v[2:17]
	ds_read_b128 v[130:133], v210 offset:7168
	v_fma_f32 v146, -v146, v18, v18
	v_fma_f32 v147, -v147, v19, v19
	ds_read_b128 v[18:21], v231 offset:36928
	ds_read_b128 v[22:25], v231 offset:36944
	ds_read_b128 v[26:29], v231 offset:36960
	ds_read_b128 v[30:33], v231 offset:36976
	v_pk_fma_f32 v[220:221], v[152:153], v[200:201], v[146:147]
	v_pk_fma_f32 v[142:143], v[148:149], v[150:151], v[150:151] neg_lo:[1,0,0] neg_hi:[1,0,0]
	s_nop 0
	v_pk_fma_f32 v[222:223], v[174:175], v[198:199], v[142:143]
	v_mfma_f32_32x32x16_bf16 v[2:17], v[46:49], v[154:157], v[2:17]
	ds_read_b128 v[146:149], v216 offset:16384
	v_add_f32_e32 v142, 1.0, v180
	v_exp_f32_e32 v143, v221
	v_exp_f32_e32 v144, v220
	v_exp_f32_e32 v145, v223
	v_exp_f32_e32 v180, v222
	v_add_f32_e32 v154, 1.0, v181
	v_add_f32_e32 v155, 1.0, v176
	v_add_f32_e32 v156, 1.0, v177
	v_mfma_f32_32x32x16_bf16 v[2:17], v[42:45], v[158:161], v[2:17]
	ds_read_b128 v[150:153], v216 offset:16416
	v_fmac_f32_e32 v142, v142, v143
	v_fmac_f32_e32 v154, v154, v144
	v_fmac_f32_e32 v155, v155, v145
	v_fmac_f32_e32 v156, v156, v180
	v_mfma_f32_32x32x16_bf16 v[2:17], v[38:41], v[186:189], v[2:17]
	ds_read_b128 v[174:177], v216 offset:16448
	v_rcp_f32_e32 v142, v142
	v_rcp_f32_e32 v154, v154
	v_mfma_f32_32x32x16_bf16 v[2:17], v[34:37], v[190:193], v[2:17]
	ds_read_b128 v[198:201], v216 offset:16480
	v_rcp_f32_e32 v155, v155
	v_rcp_f32_e32 v156, v156
	v_fma_f32 v142, -v143, v142, v142
	v_fma_f32 v143, -v144, v154, v154
	s_waitcnt lgkmcnt(4)
	v_mfma_f32_32x32x16_bf16 v[18:33], v[126:129], v[202:205], v[18:33]
	v_fma_f32 v144, -v145, v155, v155
	v_fma_f32 v145, -v180, v156, v156
	v_cvt_pk_bf16_f32 v252, v142, v143
	v_cvt_pk_bf16_f32 v253, v144, v145
	v_mfma_f32_32x32x16_bf16 v[18:33], v[122:125], v[194:197], v[18:33]
	s_nop 1
	v_exp_f32_e32 v143, v4
	v_exp_f32_e32 v142, v8
	v_exp_f32_e32 v145, v12
	v_exp_f32_e32 v144, v16
	v_mfma_f32_32x32x16_bf16 v[18:33], v[118:121], v[138:141], v[18:33]
	v_exp_f32_e32 v2, v2
	v_exp_f32_e32 v6, v6
	v_exp_f32_e32 v10, v10
	v_exp_f32_e32 v12, v14
	v_fma_f32 v4, v143, s12, s12
	v_fma_f32 v8, v142, s12, s12
	v_fma_f32 v14, v145, s12, s12
	v_fma_f32 v16, v144, s12, s12
	v_mfma_f32_32x32x16_bf16 v[18:33], v[114:117], v[134:137], v[18:33]
	v_exp_f32_e32 v3, v3
	v_fmac_f32_e32 v4, v2, v4
	v_exp_f32_e32 v2, v7
	v_fmac_f32_e32 v8, v6, v8
	v_exp_f32_e32 v6, v11
	v_exp_f32_e32 v7, v15
	v_fmac_f32_e32 v14, v10, v14
	v_fmac_f32_e32 v16, v12, v16
	v_mfma_f32_32x32x16_bf16 v[18:33], v[110:113], v[166:169], v[18:33]
	v_add_f32_e32 v10, 1.0, v3
	v_rcp_f32_e32 v3, v4
	v_add_f32_e32 v4, 1.0, v2
	v_rcp_f32_e32 v2, v8
	v_rcp_f32_e32 v155, v14
	v_rcp_f32_e32 v154, v16
	v_mfma_f32_32x32x16_bf16 v[18:33], v[106:109], v[162:165], v[18:33]
	v_add_f32_e32 v6, 1.0, v6
	v_add_f32_e32 v7, 1.0, v7
	v_rcp_f32_e32 v157, v10
	v_rcp_f32_e32 v156, v4
	v_exp_f32_e32 v160, v5
	v_exp_f32_e32 v161, v9
	v_mfma_f32_32x32x16_bf16 v[18:33], v[102:105], v[170:173], v[18:33]
	v_rcp_f32_e32 v159, v6
	v_rcp_f32_e32 v158, v7
	v_exp_f32_e32 v180, v13
	v_exp_f32_e32 v181, v17
	v_mfma_f32_32x32x16_bf16 v[18:33], v[98:101], v[130:133], v[18:33]
	v_fma_f32 v142, -v142, v2, v2
	v_fma_f32 v143, -v143, v3, v3
	v_pk_fma_f32 v[216:217], v[156:157], v[206:207], v[142:143]
	s_nop 0
	v_pk_fma_f32 v[142:143], v[144:145], v[154:155], v[154:155] neg_lo:[1,0,0] neg_hi:[1,0,0]
	s_nop 0
	v_pk_fma_f32 v[218:219], v[158:159], v[208:209], v[142:143]
	s_waitcnt lgkmcnt(0)
	v_mfma_f32_32x32x16_bf16 v[18:33], v[94:97], v[146:149], v[18:33]
	v_add_f32_e32 v142, 1.0, v160
	v_exp_f32_e32 v143, v217
	v_add_f32_e32 v144, 1.0, v161
	v_exp_f32_e32 v145, v216
	v_exp_f32_e32 v154, v219
	v_exp_f32_e32 v155, v218
	v_add_f32_e32 v156, 1.0, v180
	v_add_f32_e32 v157, 1.0, v181
	v_mfma_f32_32x32x16_bf16 v[18:33], v[90:93], v[150:153], v[18:33]
	v_fmac_f32_e32 v142, v142, v143
	v_fmac_f32_e32 v144, v144, v145
	v_fmac_f32_e32 v156, v156, v154
	v_fmac_f32_e32 v157, v157, v155
	v_mfma_f32_32x32x16_bf16 v[18:33], v[86:89], v[174:177], v[18:33]
	v_rcp_f32_e32 v142, v142
	v_rcp_f32_e32 v144, v144
	v_rcp_f32_e32 v156, v156
	v_rcp_f32_e32 v157, v157
	v_mfma_f32_32x32x16_bf16 v[18:33], v[82:85], v[198:201], v[18:33]
	v_fma_f32 v142, -v143, v142, v142
	v_fma_f32 v143, -v145, v144, v144
	v_fma_f32 v144, -v154, v156, v156
	v_fma_f32 v145, -v155, v157, v157
	v_cvt_pk_bf16_f32 v254, v142, v143
	v_cvt_pk_bf16_f32 v255, v144, v145
	ds_write_b128 v211, v[252:255] offset:8192
	s_waitcnt lgkmcnt(0)
	s_barrier
	v_mfma_f32_32x32x16_bf16 v[2:17], v[78:81], v[202:205], v[236:251]
	v_add_u32_e32 v234, v230, v229
	ds_read2_b32 v[228:229], v232 offset0:64 offset1:96
	ds_read_b128 v[206:209], v210 offset:8192
	v_mfma_f32_32x32x16_bf16 v[2:17], v[74:77], v[194:197], v[2:17]
	ds_read_b128 v[190:193], v210 offset:9216
	v_exp_f32_e32 v179, v20
	v_exp_f32_e32 v178, v24
	v_exp_f32_e32 v181, v28
	v_exp_f32_e32 v180, v32
	v_mfma_f32_32x32x16_bf16 v[2:17], v[70:73], v[138:141], v[2:17]
	ds_read_b128 v[158:161], v210 offset:10240
	v_exp_f32_e32 v18, v18
	v_exp_f32_e32 v22, v22
	v_exp_f32_e32 v24, v26
	v_exp_f32_e32 v26, v30
	v_fma_f32 v20, v179, s12, s12
	v_fma_f32 v28, v178, s12, s12
	v_fma_f32 v30, v181, s12, s12
	v_fma_f32 v32, v180, s12, s12
	v_mfma_f32_32x32x16_bf16 v[2:17], v[66:69], v[134:137], v[2:17]
	ds_read_b128 v[142:145], v210 offset:11264
	v_exp_f32_e32 v19, v19
	v_exp_f32_e32 v23, v23
	v_exp_f32_e32 v27, v27
	v_exp_f32_e32 v31, v31
	v_fmac_f32_e32 v20, v18, v20
	v_fmac_f32_e32 v28, v22, v28
	v_fmac_f32_e32 v30, v24, v30
	v_fmac_f32_e32 v32, v26, v32
	v_mfma_f32_32x32x16_bf16 v[2:17], v[62:65], v[166:169], v[2:17]
	ds_read_b128 v[154:157], v210 offset:12288
	v_add_f32_e32 v22, 1.0, v19
	v_rcp_f32_e32 v19, v20
	v_rcp_f32_e32 v18, v28
	v_rcp_f32_e32 v139, v30
	v_rcp_f32_e32 v138, v32
	v_add_f32_e32 v20, 1.0, v23
	v_mfma_f32_32x32x16_bf16 v[2:17], v[58:61], v[162:165], v[2:17]
	ds_read_b128 v[182:185], v210 offset:13312
	v_rcp_f32_e32 v141, v22
	v_rcp_f32_e32 v140, v20
	v_add_f32_e32 v23, 1.0, v27
	v_add_f32_e32 v20, 1.0, v31
	v_exp_f32_e32 v168, v21
	v_exp_f32_e32 v169, v25
	v_mfma_f32_32x32x16_bf16 v[2:17], v[54:57], v[170:173], v[2:17]
	ds_read_b128 v[186:189], v210 offset:14336
	v_rcp_f32_e32 v163, v23
	v_rcp_f32_e32 v162, v20
	v_exp_f32_e32 v194, v29
	v_exp_f32_e32 v195, v33
	v_mfma_f32_32x32x16_bf16 v[2:17], v[50:53], v[130:133], v[2:17]
	ds_read_b128 v[134:137], v210 offset:15360
	v_fma_f32 v166, -v178, v18, v18
	v_fma_f32 v167, -v179, v19, v19
	ds_read_b128 v[18:21], v231 offset:36928
	ds_read_b128 v[22:25], v231 offset:36944
	ds_read_b128 v[26:29], v231 offset:36960
	ds_read_b128 v[30:33], v231 offset:36976
	v_pk_fma_f32 v[214:215], v[140:141], v[214:215], v[166:167]
	v_pk_fma_f32 v[130:131], v[180:181], v[138:139], v[138:139] neg_lo:[1,0,0] neg_hi:[1,0,0]
	s_nop 0
	v_pk_fma_f32 v[212:213], v[162:163], v[212:213], v[130:131]
	v_mfma_f32_32x32x16_bf16 v[2:17], v[46:49], v[146:149], v[2:17]
	ds_read_b128 v[138:141], v234 offset:16384
	v_add_f32_e32 v130, 1.0, v168
	v_exp_f32_e32 v131, v215
	v_exp_f32_e32 v132, v214
	v_exp_f32_e32 v133, v213
	v_exp_f32_e32 v162, v212
	v_add_f32_e32 v163, 1.0, v169
	v_add_f32_e32 v166, 1.0, v194
	v_add_f32_e32 v167, 1.0, v195
	v_mfma_f32_32x32x16_bf16 v[2:17], v[42:45], v[150:153], v[2:17]
	ds_read_b128 v[146:149], v234 offset:16416
	v_fmac_f32_e32 v130, v130, v131
	v_fmac_f32_e32 v163, v163, v132
	v_fmac_f32_e32 v166, v166, v133
	v_fmac_f32_e32 v167, v167, v162
	v_mfma_f32_32x32x16_bf16 v[2:17], v[38:41], v[174:177], v[2:17]
	ds_read_b128 v[150:153], v234 offset:16448
	v_rcp_f32_e32 v130, v130
	v_rcp_f32_e32 v163, v163
	v_mfma_f32_32x32x16_bf16 v[2:17], v[34:37], v[198:201], v[2:17]
	ds_read_b128 v[178:181], v234 offset:16480
	v_rcp_f32_e32 v166, v166
	v_rcp_f32_e32 v167, v167
	v_fma_f32 v130, -v131, v130, v130
	v_fma_f32 v131, -v132, v163, v163
	s_waitcnt lgkmcnt(4)
	v_mfma_f32_32x32x16_bf16 v[18:33], v[126:129], v[206:209], v[18:33]
	v_fma_f32 v132, -v133, v166, v166
	v_fma_f32 v133, -v162, v167, v167
	v_cvt_pk_bf16_f32 v252, v130, v131
	v_cvt_pk_bf16_f32 v253, v132, v133
	v_mfma_f32_32x32x16_bf16 v[18:33], v[122:125], v[190:193], v[18:33]
	s_nop 1
	v_exp_f32_e32 v131, v4
	v_exp_f32_e32 v130, v8
	v_exp_f32_e32 v133, v12
	v_exp_f32_e32 v132, v16
	v_mfma_f32_32x32x16_bf16 v[18:33], v[118:121], v[158:161], v[18:33]
	v_exp_f32_e32 v2, v2
	v_exp_f32_e32 v6, v6
	v_exp_f32_e32 v10, v10
	v_exp_f32_e32 v12, v14
	v_fma_f32 v4, v131, s12, s12
	v_fma_f32 v8, v130, s12, s12
	v_fma_f32 v14, v133, s12, s12
	v_fma_f32 v16, v132, s12, s12
	v_mfma_f32_32x32x16_bf16 v[18:33], v[114:117], v[142:145], v[18:33]
	v_exp_f32_e32 v3, v3
	v_fmac_f32_e32 v4, v2, v4
	v_exp_f32_e32 v2, v7
	v_fmac_f32_e32 v8, v6, v8
	v_exp_f32_e32 v6, v11
	v_exp_f32_e32 v7, v15
	v_fmac_f32_e32 v14, v10, v14
	v_fmac_f32_e32 v16, v12, v16
	v_mfma_f32_32x32x16_bf16 v[18:33], v[110:113], v[154:157], v[18:33]
	v_add_f32_e32 v10, 1.0, v3
	v_rcp_f32_e32 v3, v4
	v_add_f32_e32 v4, 1.0, v2
	v_rcp_f32_e32 v2, v8
	v_rcp_f32_e32 v163, v14
	v_rcp_f32_e32 v162, v16
	v_mfma_f32_32x32x16_bf16 v[18:33], v[106:109], v[182:185], v[18:33]
	v_add_f32_e32 v6, 1.0, v6
	v_add_f32_e32 v7, 1.0, v7
	v_rcp_f32_e32 v167, v10
	v_rcp_f32_e32 v166, v4
	v_exp_f32_e32 v170, v5
	v_exp_f32_e32 v171, v9
	v_mfma_f32_32x32x16_bf16 v[18:33], v[102:105], v[186:189], v[18:33]
	v_rcp_f32_e32 v169, v6
	v_rcp_f32_e32 v168, v7
	v_exp_f32_e32 v172, v13
	v_exp_f32_e32 v173, v17
	v_mfma_f32_32x32x16_bf16 v[18:33], v[98:101], v[134:137], v[18:33]
	v_fma_f32 v130, -v130, v2, v2
	v_fma_f32 v131, -v131, v3, v3
	v_pk_fma_f32 v[204:205], v[166:167], v[224:225], v[130:131]
	s_nop 0
	v_pk_fma_f32 v[130:131], v[132:133], v[162:163], v[162:163] neg_lo:[1,0,0] neg_hi:[1,0,0]
	s_nop 0
	v_pk_fma_f32 v[202:203], v[168:169], v[226:227], v[130:131]
	s_waitcnt lgkmcnt(0)
	v_mfma_f32_32x32x16_bf16 v[18:33], v[94:97], v[138:141], v[18:33]
	v_add_f32_e32 v130, 1.0, v170
	v_exp_f32_e32 v131, v205
	v_add_f32_e32 v132, 1.0, v171
	v_exp_f32_e32 v133, v204
	v_exp_f32_e32 v162, v203
	v_exp_f32_e32 v163, v202
	v_add_f32_e32 v164, 1.0, v172
	v_add_f32_e32 v165, 1.0, v173
	v_mfma_f32_32x32x16_bf16 v[18:33], v[90:93], v[146:149], v[18:33]
	v_fmac_f32_e32 v130, v130, v131
	v_fmac_f32_e32 v132, v132, v133
	v_fmac_f32_e32 v164, v164, v162
	v_fmac_f32_e32 v165, v165, v163
	v_mfma_f32_32x32x16_bf16 v[18:33], v[86:89], v[150:153], v[18:33]
	v_rcp_f32_e32 v130, v130
	v_rcp_f32_e32 v132, v132
	v_rcp_f32_e32 v164, v164
	v_rcp_f32_e32 v165, v165
	v_mfma_f32_32x32x16_bf16 v[18:33], v[82:85], v[178:181], v[18:33]
	v_fma_f32 v130, -v131, v130, v130
	v_fma_f32 v131, -v133, v132, v132
	v_fma_f32 v132, -v162, v164, v164
	v_fma_f32 v133, -v163, v165, v165
	v_cvt_pk_bf16_f32 v254, v130, v131
	v_cvt_pk_bf16_f32 v255, v132, v133
	ds_write_b128 v211, v[252:255] offset:0
	s_waitcnt lgkmcnt(0)
	s_barrier
	s_branch .LBB1_13
